# all edits stacked: prep patches, one-pass LN + permlane, packed adds, silu of tiles 2-5 under GEMM2 MFMAs, scale broadcast via permlane16_swap
# baseline (speedup 1.0000x reference)
.LBB1_6:
	s_waitcnt vmcnt(14)
	ds_write_b128 v119, v[38:41]
	s_waitcnt vmcnt(13)
	ds_write_b128 v119, v[42:45] offset:2304
	s_waitcnt vmcnt(12)
	ds_write_b128 v119, v[46:49] offset:4608
	s_waitcnt vmcnt(11)
	ds_write_b128 v119, v[50:53] offset:6912
	ds_bpermute_b32 v42, v107, v64
	ds_bpermute_b32 v43, v109, v64
	ds_bpermute_b32 v44, v110, v64
	v_add_u32_e32 v0, 0x1000, v62
	ds_bpermute_b32 v50, v111, v64
	v_min_i32_e32 v0, 0x927b, v0
	v_lshl_or_b32 v40, v0, 4, v106
	s_waitcnt lgkmcnt(3)
	v_lshlrev_b32_e32 v0, 7, v42
	v_ashrrev_i32_e32 v65, 31, v64
	v_lshl_add_u64 v[46:47], v[98:99], 0, v[0:1]
	s_waitcnt lgkmcnt(2)
	v_lshlrev_b32_e32 v0, 7, v43
	v_lshl_add_u64 v[38:39], v[64:65], 2, v[96:97]
	v_ashrrev_i32_e32 v41, 31, v40
	v_lshl_add_u64 v[48:49], v[98:99], 0, v[0:1]
	s_waitcnt lgkmcnt(1)
	v_lshlrev_b32_e32 v0, 7, v44
	s_waitcnt vmcnt(10)
	v_mov_b32_e32 v68, v108
	v_mov_b32_e32 v66, v108
	s_nop 1
	v_permlane16_swap_b32_e32 v68, v66
	global_load_dword v108, v[38:39], off
	v_lshl_add_u64 v[38:39], v[40:41], 2, v[94:95]
	v_lshl_add_u64 v[64:65], v[100:101], 0, v[0:1]
	s_waitcnt lgkmcnt(0)
	v_lshlrev_b32_e32 v0, 7, v50
	global_load_dword v135, v[38:39], off
	s_nop 0
	global_load_dwordx4 v[38:41], v[46:47], off
	global_load_dwordx4 v[42:45], v[48:49], off
	v_lshl_add_u64 v[70:71], v[100:101], 0, v[0:1]
	global_load_dwordx4 v[46:49], v[64:65], off
	global_load_dwordx4 v[50:53], v[70:71], off
	ds_read_b128 v[70:73], v120
	ds_read_b128 v[74:77], v120 offset:64
	ds_read_b128 v[78:81], v120 offset:4608
	ds_read_b128 v[82:85], v120 offset:4672
	v_add_u32_e32 v0, 0x800, v62
	ds_write_b128 v121, v[2:5]
	ds_write_b128 v121, v[6:9] offset:1088
	ds_write_b128 v121, v[10:13] offset:2176
	ds_write_b128 v121, v[14:17] offset:3264
	ds_write_b128 v121, v[18:21] offset:4352
	ds_write_b128 v121, v[22:25] offset:5440
	s_waitcnt vmcnt(15)
	ds_write_b128 v121, v[26:29] offset:6528
	s_waitcnt vmcnt(14)
	ds_write_b128 v121, v[30:33] offset:7616
	ds_write_b128 v122, v[34:37] offset:8704
	v_min_i32_e32 v2, 0x927b, v0
	v_ashrrev_i32_e32 v3, 31, v2
	v_lshlrev_b64 v[4:5], 13, v[2:3]
	v_lshlrev_b64 v[2:3], 10, v[2:3]
	v_lshl_add_u64 v[18:19], v[102:103], 0, v[4:5]
	v_lshl_add_u64 v[62:63], v[104:105], 0, v[2:3]
	v_add_co_u32_e32 v64, vcc, s3, v18
	global_load_dwordx4 v[2:5], v[18:19], off nt
	global_load_dwordx4 v[6:9], v[18:19], off offset:1024 nt
	global_load_dwordx4 v[10:13], v[18:19], off offset:2048 nt
	global_load_dwordx4 v[14:17], v[18:19], off offset:3072 nt
	v_addc_co_u32_e32 v65, vcc, 0, v19, vcc
	global_load_dwordx4 v[34:37], v[62:63], off nt
	global_load_dwordx4 v[18:21], v[64:65], off nt
	global_load_dwordx4 v[22:25], v[64:65], off offset:1024 nt
	global_load_dwordx4 v[26:29], v[64:65], off offset:2048 nt
	global_load_dwordx4 v[30:33], v[64:65], off offset:3072 nt
	s_waitcnt lgkmcnt(13)
	v_add_f32_e32 v67, v68, v66
	v_mul_f32_e32 v184, 0xc3000000, v67
	s_waitcnt lgkmcnt(12)
	v_cvt_f32_ubyte3_e32 v169, v70
	v_cvt_f32_ubyte2_e32 v168, v70
	v_cvt_f32_ubyte1_e32 v171, v70
	v_cvt_f32_ubyte0_e32 v170, v70
	ds_read_b128 v[62:65], v123
	ds_read_b128 v[86:89], v123 offset:64
	ds_read_b128 v[90:93], v112
	ds_read_b128 v[136:139], v112 offset:4608
	ds_read_b128 v[140:143], v112 offset:9216
	ds_read_b128 v[144:147], v112 offset:13824
	ds_read_b128 v[148:151], v112 offset:18432
	ds_read_b128 v[152:155], v112 offset:23040
	ds_read_b128 v[156:159], v112 offset:27648
	ds_read_b128 v[160:163], v112 offset:32256
	s_waitcnt lgkmcnt(14)
	v_cvt_f32_ubyte1_e32 v165, v78
	v_cvt_f32_ubyte0_e32 v164, v78
	v_cvt_f32_ubyte3_e32 v167, v78
	v_cvt_f32_ubyte2_e32 v166, v78
	v_pk_fma_f32 v[170:171], v[170:171], v[68:69], v[184:185] op_sel_hi:[1,0,0]
	v_pk_fma_f32 v[168:169], v[168:169], v[68:69], v[184:185] op_sel_hi:[1,0,0]
	v_pk_fma_f32 v[164:165], v[164:165], v[66:67], v[170:171] op_sel_hi:[1,0,1]
	v_pk_fma_f32 v[166:167], v[166:167], v[66:67], v[168:169] op_sel_hi:[1,0,1]
	v_cvt_f32_ubyte1_e32 v169, v79
	v_cvt_f32_ubyte0_e32 v168, v79
	v_cvt_f32_ubyte3_e32 v171, v79
	v_cvt_f32_ubyte2_e32 v170, v79
	v_cvt_f32_ubyte3_e32 v79, v71
	v_cvt_f32_ubyte2_e32 v78, v71
	v_cvt_f32_ubyte1_e32 v173, v71
	v_cvt_f32_ubyte0_e32 v172, v71
	v_pk_fma_f32 v[70:71], v[172:173], v[68:69], v[184:185] op_sel_hi:[1,0,0]
	v_pk_fma_f32 v[78:79], v[78:79], v[68:69], v[184:185] op_sel_hi:[1,0,0]
	v_cvt_f32_ubyte3_e32 v173, v72
	v_cvt_f32_ubyte2_e32 v172, v72
	v_cvt_f32_ubyte1_e32 v175, v72
	v_cvt_f32_ubyte0_e32 v174, v72
	v_pk_fma_f32 v[170:171], v[170:171], v[66:67], v[78:79] op_sel_hi:[1,0,1]
	v_pk_fma_f32 v[168:169], v[168:169], v[66:67], v[70:71] op_sel_hi:[1,0,1]
	v_cvt_f32_ubyte1_e32 v71, v80
	v_cvt_f32_ubyte0_e32 v70, v80
	v_cvt_f32_ubyte3_e32 v79, v80
	v_cvt_f32_ubyte2_e32 v78, v80
	v_pk_fma_f32 v[176:177], v[174:175], v[68:69], v[184:185] op_sel_hi:[1,0,0]
	v_pk_fma_f32 v[172:173], v[172:173], v[68:69], v[184:185] op_sel_hi:[1,0,0]
	v_cvt_f32_ubyte2_e32 v80, v73
	v_pk_fma_f32 v[174:175], v[78:79], v[66:67], v[172:173] op_sel_hi:[1,0,1]
	v_pk_fma_f32 v[172:173], v[70:71], v[66:67], v[176:177] op_sel_hi:[1,0,1]
	v_cvt_f32_ubyte1_e32 v177, v73
	v_cvt_f32_ubyte0_e32 v176, v73
	v_cvt_f32_ubyte1_e32 v71, v81
	v_cvt_f32_ubyte0_e32 v70, v81
	v_cvt_f32_ubyte3_e32 v79, v81
	v_cvt_f32_ubyte2_e32 v78, v81
	v_cvt_f32_ubyte3_e32 v81, v73
	v_pk_fma_f32 v[176:177], v[176:177], v[68:69], v[184:185] op_sel_hi:[1,0,0]
	v_pk_fma_f32 v[72:73], v[80:81], v[68:69], v[184:185] op_sel_hi:[1,0,0]
	v_pk_fma_f32 v[70:71], v[70:71], v[66:67], v[176:177] op_sel_hi:[1,0,1]
	v_cvt_f32_ubyte3_e32 v177, v74
	v_cvt_f32_ubyte2_e32 v176, v74
	v_cvt_f32_ubyte1_e32 v179, v74
	v_cvt_f32_ubyte0_e32 v178, v74
	v_pk_fma_f32 v[72:73], v[78:79], v[66:67], v[72:73] op_sel_hi:[1,0,1]
	v_cvt_f32_ubyte1_e32 v79, v82
	v_cvt_f32_ubyte0_e32 v78, v82
	v_cvt_f32_ubyte3_e32 v81, v82
	v_cvt_f32_ubyte2_e32 v80, v82
	v_pk_fma_f32 v[178:179], v[178:179], v[68:69], v[184:185] op_sel_hi:[1,0,0]
	v_pk_fma_f32 v[176:177], v[176:177], v[68:69], v[184:185] op_sel_hi:[1,0,0]
	v_pk_fma_f32 v[78:79], v[78:79], v[66:67], v[178:179] op_sel_hi:[1,0,1]
	v_pk_fma_f32 v[80:81], v[80:81], v[66:67], v[176:177] op_sel_hi:[1,0,1]
	v_cvt_f32_ubyte1_e32 v177, v83
	v_cvt_f32_ubyte0_e32 v176, v83
	v_cvt_f32_ubyte3_e32 v179, v83
	v_cvt_f32_ubyte2_e32 v178, v83
	v_cvt_f32_ubyte3_e32 v83, v75
	v_cvt_f32_ubyte2_e32 v82, v75
	v_cvt_f32_ubyte1_e32 v181, v75
	v_cvt_f32_ubyte0_e32 v180, v75
	v_pk_fma_f32 v[74:75], v[180:181], v[68:69], v[184:185] op_sel_hi:[1,0,0]
	v_pk_fma_f32 v[82:83], v[82:83], v[68:69], v[184:185] op_sel_hi:[1,0,0]
	v_cvt_f32_ubyte3_e32 v181, v76
	v_cvt_f32_ubyte2_e32 v180, v76
	v_cvt_f32_ubyte1_e32 v183, v76
	v_cvt_f32_ubyte0_e32 v182, v76
	v_pk_fma_f32 v[178:179], v[178:179], v[66:67], v[82:83] op_sel_hi:[1,0,1]
	v_pk_fma_f32 v[176:177], v[176:177], v[66:67], v[74:75] op_sel_hi:[1,0,1]
	v_cvt_f32_ubyte1_e32 v75, v84
	v_cvt_f32_ubyte0_e32 v74, v84
	v_cvt_f32_ubyte3_e32 v83, v84
	v_cvt_f32_ubyte2_e32 v82, v84
	v_pk_fma_f32 v[186:187], v[182:183], v[68:69], v[184:185] op_sel_hi:[1,0,0]
	v_pk_fma_f32 v[180:181], v[180:181], v[68:69], v[184:185] op_sel_hi:[1,0,0]
	v_cvt_f32_ubyte2_e32 v84, v77
	v_pk_fma_f32 v[182:183], v[82:83], v[66:67], v[180:181] op_sel_hi:[1,0,1]
	v_pk_fma_f32 v[180:181], v[74:75], v[66:67], v[186:187] op_sel_hi:[1,0,1]
	v_cvt_f32_ubyte1_e32 v75, v85
	v_cvt_f32_ubyte0_e32 v74, v85
	v_cvt_f32_ubyte3_e32 v83, v85
	v_cvt_f32_ubyte2_e32 v82, v85
	v_cvt_f32_ubyte3_e32 v85, v77
	v_cvt_f32_ubyte1_e32 v187, v77
	v_cvt_f32_ubyte0_e32 v186, v77
	v_pk_fma_f32 v[76:77], v[186:187], v[68:69], v[184:185] op_sel_hi:[1,0,0]
	v_pk_fma_f32 v[68:69], v[84:85], v[68:69], v[184:185] op_sel_hi:[1,0,0]
	s_nop 0
	v_pk_fma_f32 v[68:69], v[82:83], v[66:67], v[68:69] op_sel_hi:[1,0,1]
	v_pk_fma_f32 v[66:67], v[74:75], v[66:67], v[76:77] op_sel_hi:[1,0,1]
	ds_read_b128 v[74:77], v123 offset:128
	ds_read_b128 v[82:85], v123 offset:192
	ds_read_b128 v[184:187], v112 offset:64
	ds_read_b128 v[188:191], v112 offset:4672
	ds_read_b128 v[192:195], v112 offset:9280
	ds_read_b128 v[196:199], v112 offset:13888
	ds_read_b128 v[200:203], v112 offset:18496
	ds_read_b128 v[204:207], v112 offset:23104
	ds_read_b128 v[208:211], v112 offset:27712
	ds_read_b128 v[212:215], v112 offset:32320
	s_waitcnt lgkmcnt(14)
	v_cvt_pk_bf16_f32 v62, v62, v63
	v_cvt_pk_bf16_f32 v63, v64, v65
	v_cvt_pk_bf16_f32 v64, v86, v87
	v_cvt_pk_bf16_f32 v65, v88, v89
	s_nop 1
	v_mfma_f32_16x16x32_bf16 v[86:89], v[90:93], v[62:65], v[164:167]
	v_mfma_f32_16x16x32_bf16 v[90:93], v[136:139], v[62:65], v[168:171]
	v_mfma_f32_16x16x32_bf16 v[136:139], v[140:143], v[62:65], v[172:175]
	v_mfma_f32_16x16x32_bf16 v[70:73], v[144:147], v[62:65], v[70:73]
	s_waitcnt lgkmcnt(13)
	v_mfma_f32_16x16x32_bf16 v[78:81], v[148:151], v[62:65], v[78:81]
	s_waitcnt lgkmcnt(12)
	v_mfma_f32_16x16x32_bf16 v[140:143], v[152:155], v[62:65], v[176:179]
	s_waitcnt lgkmcnt(11)
	v_mfma_f32_16x16x32_bf16 v[144:147], v[156:159], v[62:65], v[180:183]
	s_waitcnt lgkmcnt(10)
	v_mfma_f32_16x16x32_bf16 v[62:65], v[160:163], v[62:65], v[66:69]
	s_nop 2
	ds_read_b128 v[66:69], v123 offset:256
	ds_read_b128 v[148:151], v123 offset:320
	ds_read_b128 v[152:155], v112 offset:128
	ds_read_b128 v[156:159], v112 offset:4736
	ds_read_b128 v[160:163], v112 offset:9344
	ds_read_b128 v[164:167], v112 offset:13952
	ds_read_b128 v[168:171], v112 offset:18560
	ds_read_b128 v[172:175], v112 offset:23168
	ds_read_b128 v[176:179], v112 offset:27776
	ds_read_b128 v[180:183], v112 offset:32384
	s_waitcnt lgkmcnt(14)
	v_cvt_pk_bf16_f32 v74, v74, v75
	v_cvt_pk_bf16_f32 v75, v76, v77
	v_cvt_pk_bf16_f32 v76, v82, v83
	v_cvt_pk_bf16_f32 v77, v84, v85
	s_waitcnt lgkmcnt(10)
	s_nop 0
	v_mfma_f32_16x16x32_bf16 v[62:65], v[212:215], v[74:77], v[62:65]
	v_mfma_f32_16x16x32_bf16 v[82:85], v[184:187], v[74:77], v[86:89]
	v_mfma_f32_16x16x32_bf16 v[86:89], v[188:191], v[74:77], v[90:93]
	v_mfma_f32_16x16x32_bf16 v[90:93], v[192:195], v[74:77], v[136:139]
	v_mfma_f32_16x16x32_bf16 v[70:73], v[196:199], v[74:77], v[70:73]
	v_mfma_f32_16x16x32_bf16 v[78:81], v[200:203], v[74:77], v[78:81]
	v_mfma_f32_16x16x32_bf16 v[136:139], v[204:207], v[74:77], v[140:143]
	v_mfma_f32_16x16x32_bf16 v[140:143], v[208:211], v[74:77], v[144:147]
	ds_read_b128 v[74:77], v123 offset:384
	s_nop 1
	ds_read_b128 v[144:147], v123 offset:448
	ds_read_b128 v[184:187], v112 offset:192
	ds_read_b128 v[188:191], v112 offset:4800
	ds_read_b128 v[192:195], v112 offset:9408
	ds_read_b128 v[196:199], v112 offset:14016
	ds_read_b128 v[200:203], v112 offset:18624
	ds_read_b128 v[204:207], v112 offset:23232
	ds_read_b128 v[208:211], v112 offset:27840
	ds_read_b128 v[212:215], v112 offset:32448
	s_waitcnt lgkmcnt(14)
	v_cvt_pk_bf16_f32 v66, v66, v67
	v_cvt_pk_bf16_f32 v67, v68, v69
	v_cvt_pk_bf16_f32 v68, v148, v149
	v_cvt_pk_bf16_f32 v69, v150, v151
	s_waitcnt lgkmcnt(10)
	s_nop 0
	v_mfma_f32_16x16x32_bf16 v[62:65], v[180:183], v[66:69], v[62:65]
	v_mfma_f32_16x16x32_bf16 v[82:85], v[152:155], v[66:69], v[82:85]
	v_mfma_f32_16x16x32_bf16 v[86:89], v[156:159], v[66:69], v[86:89]
	v_mfma_f32_16x16x32_bf16 v[90:93], v[160:163], v[66:69], v[90:93]
	v_mfma_f32_16x16x32_bf16 v[70:73], v[164:167], v[66:69], v[70:73]
	v_mfma_f32_16x16x32_bf16 v[78:81], v[168:171], v[66:69], v[78:81]
	v_mfma_f32_16x16x32_bf16 v[136:139], v[172:175], v[66:69], v[136:139]
	v_mfma_f32_16x16x32_bf16 v[140:143], v[176:179], v[66:69], v[140:143]
	ds_read2st64_b64 v[66:69], v134 offset0:54 offset1:63
	ds_read2st64_b64 v[148:151], v134 offset0:36 offset1:45
	ds_read2st64_b64 v[152:155], v134 offset0:18 offset1:27
	ds_read2st64_b64 v[156:159], v134 offset1:9
	ds_read_b128 v[160:163], v124 offset:8704
	s_waitcnt lgkmcnt(14)
	v_cvt_pk_bf16_f32 v74, v74, v75
	v_cvt_pk_bf16_f32 v75, v76, v77
	s_waitcnt lgkmcnt(13)
	v_cvt_pk_bf16_f32 v76, v144, v145
	v_cvt_pk_bf16_f32 v77, v146, v147
	s_waitcnt lgkmcnt(5)
	s_nop 0
	v_mfma_f32_16x16x32_bf16 v[62:65], v[212:215], v[74:77], v[62:65]
	v_mfma_f32_16x16x32_bf16 v[82:85], v[184:187], v[74:77], v[82:85]
	v_mfma_f32_16x16x32_bf16 v[86:89], v[188:191], v[74:77], v[86:89]
	v_mfma_f32_16x16x32_bf16 v[90:93], v[192:195], v[74:77], v[90:93]
	v_mfma_f32_16x16x32_bf16 v[70:73], v[196:199], v[74:77], v[70:73]
	v_mfma_f32_16x16x32_bf16 v[78:81], v[200:203], v[74:77], v[78:81]
	v_mfma_f32_16x16x32_bf16 v[136:139], v[204:207], v[74:77], v[136:139]
	v_mfma_f32_16x16x32_bf16 v[140:143], v[208:211], v[74:77], v[140:143]
	ds_read_b128 v[144:147], v125
	ds_read_b128 v[164:167], v126
	ds_read_b128 v[168:171], v127
	ds_read_b128 v[172:175], v128
	ds_read_b128 v[176:179], v129
	ds_read_b128 v[180:183], v130
	ds_read_b128 v[184:187], v131
	ds_read_b128 v[188:191], v132
	ds_read_b128 v[192:195], v112 offset:36864
	ds_read_b128 v[196:199], v112 offset:41472
	ds_read_b128 v[200:203], v112 offset:46080
	ds_read_b128 v[204:207], v112 offset:50688
	ds_read_b128 v[208:211], v112 offset:55296
	ds_read_b128 v[212:215], v112 offset:59904
	ds_read_b128 v[216:219], v112 offset:64512
	ds_read_b128 v[220:223], v113 offset:32256
	s_waitcnt lgkmcnt(14)
	v_cvt_pk_bf16_f32 v74, v160, v161
	v_cvt_pk_bf16_f32 v75, v162, v163
	s_nop 1
	v_mfma_f32_16x16x16_bf16 v[160:163], v[156:157], v[74:75], v[82:85]
	v_mfma_f32_16x16x16_bf16 v[86:89], v[158:159], v[74:75], v[86:89]
	v_mfma_f32_16x16x16_bf16 v[90:93], v[152:153], v[74:75], v[90:93]
	v_mfma_f32_16x16x16_bf16 v[70:73], v[154:155], v[74:75], v[70:73]
	v_mfma_f32_16x16x16_bf16 v[78:81], v[148:149], v[74:75], v[78:81]
	v_mfma_f32_16x16x16_bf16 v[136:139], v[150:151], v[74:75], v[136:139]
	v_mfma_f32_16x16x16_bf16 v[82:85], v[66:67], v[74:75], v[140:143]
	v_mfma_f32_16x16x16_bf16 v[74:77], v[68:69], v[74:75], v[62:65]
	s_nop 2
	v_exp_f32_e32 v240, v160
	v_exp_f32_e32 v241, v161
	v_exp_f32_e32 v242, v162
	v_exp_f32_e32 v243, v163
	v_pk_add_f32 v[240:241], v[240:241], 1.0 op_sel_hi:[1,0]
	v_pk_add_f32 v[242:243], v[242:243], 1.0 op_sel_hi:[1,0]
	v_rcp_f32_e32 v240, v240
	v_rcp_f32_e32 v241, v241
	v_rcp_f32_e32 v242, v242
	v_rcp_f32_e32 v243, v243
	v_pk_mul_f32 v[240:241], v[160:161], v[240:241]
	v_pk_mul_f32 v[242:243], v[162:163], v[242:243]
	v_cvt_pk_bf16_f32 v140, v240, v241
	v_cvt_pk_bf16_f32 v141, v242, v243
	v_exp_f32_e32 v244, v86
	v_exp_f32_e32 v245, v87
	v_exp_f32_e32 v246, v88
	v_exp_f32_e32 v247, v89
	v_pk_add_f32 v[244:245], v[244:245], 1.0 op_sel_hi:[1,0]
	v_pk_add_f32 v[246:247], v[246:247], 1.0 op_sel_hi:[1,0]
	v_rcp_f32_e32 v244, v244
	v_rcp_f32_e32 v245, v245
	v_rcp_f32_e32 v246, v246
	v_rcp_f32_e32 v247, v247
	v_pk_mul_f32 v[244:245], v[86:87], v[244:245]
	v_pk_mul_f32 v[246:247], v[88:89], v[246:247]
	v_cvt_pk_bf16_f32 v142, v244, v245
	v_cvt_pk_bf16_f32 v143, v246, v247
	v_mov_b32_e32 v236, v136
	v_mov_b32_e32 v237, v137
	v_mov_b32_e32 v238, v138
	v_mov_b32_e32 v239, v139
	ds_read_b128 v[248:251], v112 offset:36928
	ds_read_b128 v[136:139], v112 offset:41536
	ds_read_b128 v[152:155], v112 offset:46144
	ds_read_b128 v[156:159], v112 offset:50752
	ds_read_b128 v[160:163], v112 offset:55360
	ds_read_b128 v[224:227], v112 offset:59968
	ds_read_b128 v[228:231], v112 offset:64576
	ds_read_b128 v[232:235], v113 offset:32320
	ds_read_b128 v[62:65], v123
	ds_read_b128 v[66:69], v123 offset:64
	s_waitcnt lgkmcnt(14)
	v_mfma_f32_16x16x32_bf16 v[144:147], v[192:195], v[140:143], v[144:147]
	v_mfma_f32_16x16x32_bf16 v[164:167], v[196:199], v[140:143], v[164:167]
	v_mfma_f32_16x16x32_bf16 v[168:171], v[200:203], v[140:143], v[168:171]
	v_mfma_f32_16x16x32_bf16 v[172:175], v[204:207], v[140:143], v[172:175]
	s_waitcnt lgkmcnt(13)
	v_mfma_f32_16x16x32_bf16 v[176:179], v[208:211], v[140:143], v[176:179]
	s_waitcnt lgkmcnt(12)
	v_mfma_f32_16x16x32_bf16 v[180:183], v[212:215], v[140:143], v[180:183]
	s_waitcnt lgkmcnt(11)
	v_mfma_f32_16x16x32_bf16 v[184:187], v[216:219], v[140:143], v[184:187]
	s_waitcnt lgkmcnt(10)
	v_mfma_f32_16x16x32_bf16 v[140:143], v[220:223], v[140:143], v[188:191]
	v_exp_f32_e32 v240, v90
	v_exp_f32_e32 v241, v91
	v_exp_f32_e32 v242, v92
	v_exp_f32_e32 v243, v93
	v_pk_add_f32 v[240:241], v[240:241], 1.0 op_sel_hi:[1,0]
	v_pk_add_f32 v[242:243], v[242:243], 1.0 op_sel_hi:[1,0]
	v_rcp_f32_e32 v240, v240
	v_rcp_f32_e32 v241, v241
	v_rcp_f32_e32 v242, v242
	v_rcp_f32_e32 v243, v243
	v_pk_mul_f32 v[240:241], v[90:91], v[240:241]
	v_pk_mul_f32 v[242:243], v[92:93], v[242:243]
	v_cvt_pk_bf16_f32 v86, v240, v241
	v_cvt_pk_bf16_f32 v87, v242, v243
	v_exp_f32_e32 v244, v70
	v_exp_f32_e32 v245, v71
	v_exp_f32_e32 v246, v72
	v_exp_f32_e32 v247, v73
	v_pk_add_f32 v[244:245], v[244:245], 1.0 op_sel_hi:[1,0]
	v_pk_add_f32 v[246:247], v[246:247], 1.0 op_sel_hi:[1,0]
	v_rcp_f32_e32 v244, v244
	v_rcp_f32_e32 v245, v245
	v_rcp_f32_e32 v246, v246
	v_rcp_f32_e32 v247, v247
	v_pk_mul_f32 v[244:245], v[70:71], v[244:245]
	v_pk_mul_f32 v[246:247], v[72:73], v[246:247]
	v_cvt_pk_bf16_f32 v88, v244, v245
	v_cvt_pk_bf16_f32 v89, v246, v247
	s_nop 2
	ds_read_b128 v[188:191], v112 offset:36992
	ds_read_b128 v[192:195], v112 offset:41600
	ds_read_b128 v[196:199], v112 offset:46208
	ds_read_b128 v[200:203], v112 offset:50816
	ds_read_b128 v[204:207], v112 offset:55424
	ds_read_b128 v[208:211], v112 offset:60032
	ds_read_b128 v[212:215], v112 offset:64640
	ds_read_b128 v[216:219], v113 offset:32384
	ds_read_b128 v[70:73], v123 offset:128
	ds_read_b128 v[252:255], v123 offset:192
	s_waitcnt lgkmcnt(14)
	v_mfma_f32_16x16x32_bf16 v[144:147], v[248:251], v[86:89], v[144:147]
	v_mfma_f32_16x16x32_bf16 v[136:139], v[136:139], v[86:89], v[164:167]
	v_mfma_f32_16x16x32_bf16 v[152:155], v[152:155], v[86:89], v[168:171]
	v_mfma_f32_16x16x32_bf16 v[156:159], v[156:159], v[86:89], v[172:175]
	v_mfma_f32_16x16x32_bf16 v[160:163], v[160:163], v[86:89], v[176:179]
	v_mfma_f32_16x16x32_bf16 v[164:167], v[224:227], v[86:89], v[180:183]
	s_waitcnt lgkmcnt(13)
	v_mfma_f32_16x16x32_bf16 v[168:171], v[228:231], v[86:89], v[184:187]
	s_waitcnt lgkmcnt(12)
	v_mfma_f32_16x16x32_bf16 v[140:143], v[232:235], v[86:89], v[140:143]
	v_exp_f32_e32 v240, v78
	v_exp_f32_e32 v241, v79
	v_exp_f32_e32 v242, v80
	v_exp_f32_e32 v243, v81
	v_pk_add_f32 v[240:241], v[240:241], 1.0 op_sel_hi:[1,0]
	v_pk_add_f32 v[242:243], v[242:243], 1.0 op_sel_hi:[1,0]
	v_rcp_f32_e32 v240, v240
	v_rcp_f32_e32 v241, v241
	v_rcp_f32_e32 v242, v242
	v_rcp_f32_e32 v243, v243
	v_pk_mul_f32 v[240:241], v[78:79], v[240:241]
	v_pk_mul_f32 v[242:243], v[80:81], v[242:243]
	v_cvt_pk_bf16_f32 v148, v240, v241
	v_cvt_pk_bf16_f32 v149, v242, v243
	v_exp_f32_e32 v244, v236
	v_exp_f32_e32 v245, v237
	v_exp_f32_e32 v246, v238
	v_exp_f32_e32 v247, v239
	v_pk_add_f32 v[244:245], v[244:245], 1.0 op_sel_hi:[1,0]
	v_pk_add_f32 v[246:247], v[246:247], 1.0 op_sel_hi:[1,0]
	v_rcp_f32_e32 v244, v244
	v_rcp_f32_e32 v245, v245
	v_rcp_f32_e32 v246, v246
	v_rcp_f32_e32 v247, v247
	v_pk_mul_f32 v[244:245], v[236:237], v[244:245]
	v_pk_mul_f32 v[246:247], v[238:239], v[246:247]
	v_cvt_pk_bf16_f32 v150, v244, v245
	v_cvt_pk_bf16_f32 v151, v246, v247
	ds_read_b128 v[172:175], v112 offset:37056
	ds_read_b128 v[176:179], v112 offset:41664
	ds_read_b128 v[180:183], v112 offset:46272
	ds_read_b128 v[184:187], v112 offset:50880
	ds_read_b128 v[220:223], v112 offset:55488
	ds_read_b128 v[224:227], v112 offset:60096
	ds_read_b128 v[228:231], v112 offset:64704
	ds_read_b128 v[232:235], v113 offset:32448
	ds_read_b128 v[86:89], v123 offset:256
	ds_read_b128 v[90:93], v123 offset:320
	s_waitcnt lgkmcnt(14)
	v_mfma_f32_16x16x32_bf16 v[144:147], v[188:191], v[148:151], v[144:147]
	v_mfma_f32_16x16x32_bf16 v[136:139], v[192:195], v[148:151], v[136:139]
	v_mfma_f32_16x16x32_bf16 v[152:155], v[196:199], v[148:151], v[152:155]
	v_mfma_f32_16x16x32_bf16 v[156:159], v[200:203], v[148:151], v[156:159]
	v_mfma_f32_16x16x32_bf16 v[160:163], v[204:207], v[148:151], v[160:163]
	v_mfma_f32_16x16x32_bf16 v[164:167], v[208:211], v[148:151], v[164:167]
	s_waitcnt lgkmcnt(13)
	v_mfma_f32_16x16x32_bf16 v[168:171], v[212:215], v[148:151], v[168:171]
	s_waitcnt lgkmcnt(12)
	v_mfma_f32_16x16x32_bf16 v[140:143], v[216:219], v[148:151], v[140:143]
	v_exp_f32_e32 v148, v82
	v_exp_f32_e32 v149, v83
	v_exp_f32_e32 v150, v84
	v_exp_f32_e32 v151, v85
	v_add_f32_e32 v148, 1.0, v148
	v_add_f32_e32 v149, 1.0, v149
	v_rcp_f32_e32 v148, v148
	v_rcp_f32_e32 v149, v149
	v_add_f32_e32 v150, 1.0, v150
	v_add_f32_e32 v151, 1.0, v151
	v_rcp_f32_e32 v150, v150
	v_rcp_f32_e32 v151, v151
	v_pk_mul_f32 v[82:83], v[82:83], v[148:149]
	v_exp_f32_e32 v148, v74
	v_cvt_pk_bf16_f32 v82, v82, v83
	v_pk_mul_f32 v[84:85], v[84:85], v[150:151]
	v_exp_f32_e32 v149, v77
	v_cvt_pk_bf16_f32 v83, v84, v85
	v_exp_f32_e32 v85, v75
	v_add_f32_e32 v84, 1.0, v148
	v_exp_f32_e32 v148, v76
	v_rcp_f32_e32 v84, v84
	v_add_f32_e32 v85, 1.0, v85
	v_rcp_f32_e32 v85, v85
	v_add_f32_e32 v148, 1.0, v148
	v_rcp_f32_e32 v192, v148
	v_add_f32_e32 v148, 1.0, v149
	v_rcp_f32_e32 v193, v148
	ds_read_b128 v[148:151], v123 offset:384
	ds_read_b128 v[188:191], v123 offset:448
	v_pk_mul_f32 v[74:75], v[74:75], v[84:85]
	s_nop 0
	v_cvt_pk_bf16_f32 v84, v74, v75
	v_pk_mul_f32 v[74:75], v[76:77], v[192:193]
	s_nop 0
	v_cvt_pk_bf16_f32 v85, v74, v75
	s_waitcnt lgkmcnt(11)
	s_nop 0
	v_mfma_f32_16x16x32_bf16 v[74:77], v[172:175], v[82:85], v[144:147]
	s_waitcnt lgkmcnt(10)
	v_mfma_f32_16x16x32_bf16 v[136:139], v[176:179], v[82:85], v[136:139]
	s_waitcnt lgkmcnt(9)
	v_mfma_f32_16x16x32_bf16 v[144:147], v[180:183], v[82:85], v[152:155]
	s_waitcnt lgkmcnt(8)
	v_mfma_f32_16x16x32_bf16 v[152:155], v[184:187], v[82:85], v[156:159]
	s_waitcnt lgkmcnt(7)
	v_mfma_f32_16x16x32_bf16 v[156:159], v[220:223], v[82:85], v[160:163]
	s_waitcnt lgkmcnt(6)
	v_mfma_f32_16x16x32_bf16 v[160:163], v[224:227], v[82:85], v[164:167]
	s_waitcnt lgkmcnt(5)
	v_mfma_f32_16x16x32_bf16 v[164:167], v[228:231], v[82:85], v[168:171]
	s_waitcnt lgkmcnt(4)
	v_mfma_f32_16x16x32_bf16 v[82:85], v[232:235], v[82:85], v[140:143]
	s_nop 2
	v_exp_f32_e32 v140, v74
	v_exp_f32_e32 v141, v75
	v_exp_f32_e32 v168, v136
	v_exp_f32_e32 v169, v137
	v_exp_f32_e32 v170, v138
	v_exp_f32_e32 v171, v139
	v_exp_f32_e32 v142, v76
	v_exp_f32_e32 v143, v77
	v_add_f32_e32 v140, 1.0, v140
	v_add_f32_e32 v141, 1.0, v141
	v_rcp_f32_e32 v140, v140
	v_rcp_f32_e32 v141, v141
	v_add_f32_e32 v168, 1.0, v168
	v_add_f32_e32 v169, 1.0, v169
	v_rcp_f32_e32 v168, v168
	v_rcp_f32_e32 v169, v169
	v_pk_add_f32 v[170:171], v[170:171], 1.0 op_sel_hi:[1,0]
	v_pk_add_f32 v[142:143], v[142:143], 1.0 op_sel_hi:[1,0]
	v_rcp_f32_e32 v170, v170
	v_rcp_f32_e32 v171, v171
	v_rcp_f32_e32 v142, v142
	v_rcp_f32_e32 v143, v143
	v_exp_f32_e32 v172, v144
	v_exp_f32_e32 v173, v145
	v_pk_mul_f32 v[74:75], v[74:75], v[140:141]
	v_pk_mul_f32 v[136:137], v[136:137], v[168:169]
	v_pk_fma_f32 v[62:63], v[74:75], s[2:3], v[62:63] op_sel_hi:[1,0,1]
	v_exp_f32_e32 v174, v146
	v_pk_mul_f32 v[236:237], v[62:63], v[62:63]
	v_pk_add_f32 v[238:239], v[62:63], 0 op_sel_hi:[1,0]
	v_exp_f32_e32 v175, v147
	v_pk_fma_f32 v[66:67], v[136:137], s[2:3], v[66:67] op_sel_hi:[1,0,1]
	v_pk_mul_f32 v[136:137], v[138:139], v[170:171]
	v_pk_fma_f32 v[236:237], v[66:67], v[66:67], v[236:237]
	v_pk_add_f32 v[238:239], v[66:67], v[238:239]
	v_pk_fma_f32 v[68:69], v[136:137], s[2:3], v[68:69] op_sel_hi:[1,0,1]
	v_pk_mul_f32 v[74:75], v[76:77], v[142:143]
	v_pk_fma_f32 v[236:237], v[68:69], v[68:69], v[236:237]
	v_pk_add_f32 v[238:239], v[68:69], v[238:239]
	v_pk_add_f32 v[172:173], v[172:173], 1.0 op_sel_hi:[1,0]
	v_exp_f32_e32 v176, v152
	v_exp_f32_e32 v177, v153
	v_pk_fma_f32 v[64:65], v[74:75], s[2:3], v[64:65] op_sel_hi:[1,0,1]
	v_rcp_f32_e32 v172, v172
	v_pk_fma_f32 v[236:237], v[64:65], v[64:65], v[236:237]
	v_pk_add_f32 v[238:239], v[64:65], v[238:239]
	v_rcp_f32_e32 v173, v173
	v_pk_add_f32 v[174:175], v[174:175], 1.0 op_sel_hi:[1,0]
	v_exp_f32_e32 v178, v154
	v_exp_f32_e32 v179, v155
	v_rcp_f32_e32 v174, v174
	v_rcp_f32_e32 v175, v175
	v_pk_add_f32 v[176:177], v[176:177], 1.0 op_sel_hi:[1,0]
	v_exp_f32_e32 v180, v156
	v_exp_f32_e32 v181, v157
	v_rcp_f32_e32 v176, v176
	v_rcp_f32_e32 v177, v177
	v_pk_mul_f32 v[144:145], v[144:145], v[172:173]
	v_pk_add_f32 v[178:179], v[178:179], 1.0 op_sel_hi:[1,0]
	v_exp_f32_e32 v182, v158
	v_exp_f32_e32 v183, v159
	v_pk_fma_f32 v[70:71], v[144:145], s[2:3], v[70:71] op_sel_hi:[1,0,1]
	v_rcp_f32_e32 v178, v178
	v_pk_fma_f32 v[236:237], v[70:71], v[70:71], v[236:237]
	v_pk_add_f32 v[238:239], v[70:71], v[238:239]
	v_rcp_f32_e32 v179, v179
	v_pk_mul_f32 v[144:145], v[146:147], v[174:175]
	v_pk_add_f32 v[180:181], v[180:181], 1.0 op_sel_hi:[1,0]
	v_exp_f32_e32 v184, v160
	v_exp_f32_e32 v185, v161
	v_pk_fma_f32 v[72:73], v[144:145], s[2:3], v[72:73] op_sel_hi:[1,0,1]
	v_rcp_f32_e32 v180, v180
	v_pk_fma_f32 v[236:237], v[72:73], v[72:73], v[236:237]
	v_pk_add_f32 v[238:239], v[72:73], v[238:239]
	v_rcp_f32_e32 v181, v181
	v_pk_mul_f32 v[152:153], v[152:153], v[176:177]
	v_pk_add_f32 v[182:183], v[182:183], 1.0 op_sel_hi:[1,0]
	v_exp_f32_e32 v186, v162
	v_exp_f32_e32 v187, v163
	v_pk_fma_f32 v[78:79], v[152:153], s[2:3], v[252:253] op_sel_hi:[1,0,1]
	v_rcp_f32_e32 v182, v182
	v_pk_fma_f32 v[236:237], v[78:79], v[78:79], v[236:237]
	v_pk_add_f32 v[238:239], v[78:79], v[238:239]
	v_rcp_f32_e32 v183, v183
	v_pk_mul_f32 v[152:153], v[154:155], v[178:179]
	v_pk_add_f32 v[184:185], v[184:185], 1.0 op_sel_hi:[1,0]
	v_exp_f32_e32 v192, v164
	v_exp_f32_e32 v193, v165
	v_pk_fma_f32 v[80:81], v[152:153], s[2:3], v[254:255] op_sel_hi:[1,0,1]
	v_rcp_f32_e32 v184, v184
	v_pk_fma_f32 v[236:237], v[80:81], v[80:81], v[236:237]
	v_pk_add_f32 v[238:239], v[80:81], v[238:239]
	v_rcp_f32_e32 v185, v185
	v_pk_mul_f32 v[156:157], v[156:157], v[180:181]
	v_pk_add_f32 v[186:187], v[186:187], 1.0 op_sel_hi:[1,0]
	v_exp_f32_e32 v194, v166
	v_exp_f32_e32 v195, v167
	s_waitcnt lgkmcnt(3)
	v_pk_fma_f32 v[86:87], v[156:157], s[2:3], v[86:87] op_sel_hi:[1,0,1]
	v_rcp_f32_e32 v186, v186
	v_pk_fma_f32 v[236:237], v[86:87], v[86:87], v[236:237]
	v_pk_add_f32 v[238:239], v[86:87], v[238:239]
	v_rcp_f32_e32 v187, v187
	v_pk_mul_f32 v[156:157], v[158:159], v[182:183]
	v_pk_add_f32 v[192:193], v[192:193], 1.0 op_sel_hi:[1,0]
	v_exp_f32_e32 v196, v82
	v_exp_f32_e32 v197, v83
	v_pk_fma_f32 v[88:89], v[156:157], s[2:3], v[88:89] op_sel_hi:[1,0,1]
	v_rcp_f32_e32 v192, v192
	v_pk_fma_f32 v[236:237], v[88:89], v[88:89], v[236:237]
	v_pk_add_f32 v[238:239], v[88:89], v[238:239]
	v_rcp_f32_e32 v193, v193
	v_pk_mul_f32 v[160:161], v[160:161], v[184:185]
	v_pk_add_f32 v[194:195], v[194:195], 1.0 op_sel_hi:[1,0]
	v_exp_f32_e32 v198, v84
	v_exp_f32_e32 v199, v85
	s_waitcnt lgkmcnt(2)
	v_pk_fma_f32 v[90:91], v[160:161], s[2:3], v[90:91] op_sel_hi:[1,0,1]
	v_rcp_f32_e32 v194, v194
	v_pk_fma_f32 v[236:237], v[90:91], v[90:91], v[236:237]
	v_pk_add_f32 v[238:239], v[90:91], v[238:239]
	v_rcp_f32_e32 v195, v195
	v_pk_mul_f32 v[160:161], v[162:163], v[186:187]
	v_pk_add_f32 v[196:197], v[196:197], 1.0 op_sel_hi:[1,0]
	v_pk_fma_f32 v[92:93], v[160:161], s[2:3], v[92:93] op_sel_hi:[1,0,1]
	v_rcp_f32_e32 v196, v196
	v_pk_fma_f32 v[236:237], v[92:93], v[92:93], v[236:237]
	v_pk_add_f32 v[238:239], v[92:93], v[238:239]
	v_rcp_f32_e32 v197, v197
	v_pk_mul_f32 v[164:165], v[164:165], v[192:193]
	v_pk_add_f32 v[198:199], v[198:199], 1.0 op_sel_hi:[1,0]
	s_waitcnt lgkmcnt(1)
	v_pk_fma_f32 v[148:149], v[164:165], s[2:3], v[148:149] op_sel_hi:[1,0,1]
	v_rcp_f32_e32 v198, v198
	v_pk_fma_f32 v[236:237], v[148:149], v[148:149], v[236:237]
	v_pk_add_f32 v[238:239], v[148:149], v[238:239]
	v_rcp_f32_e32 v199, v199
	v_pk_mul_f32 v[164:165], v[166:167], v[194:195]
	s_nop 0
	v_pk_fma_f32 v[150:151], v[164:165], s[2:3], v[150:151] op_sel_hi:[1,0,1]
	v_pk_mul_f32 v[82:83], v[82:83], v[196:197]
	v_pk_fma_f32 v[236:237], v[150:151], v[150:151], v[236:237]
	v_pk_add_f32 v[238:239], v[150:151], v[238:239]
	s_waitcnt lgkmcnt(0)
	v_pk_fma_f32 v[82:83], v[82:83], s[2:3], v[188:189] op_sel_hi:[1,0,1]
	v_pk_mul_f32 v[84:85], v[84:85], v[198:199]
	v_pk_fma_f32 v[236:237], v[82:83], v[82:83], v[236:237]
	v_pk_fma_f32 v[84:85], v[84:85], s[2:3], v[190:191] op_sel_hi:[1,0,1]
	v_pk_add_f32 v[238:239], v[82:83], v[238:239]
	v_pk_fma_f32 v[236:237], v[84:85], v[84:85], v[236:237]
	v_pk_add_f32 v[238:239], v[84:85], v[238:239]
	v_add_f32_e32 v75, v236, v237
	v_add_f32_e32 v74, v238, v239
	s_nop 1
	v_permlane16_swap_b32_e32 v74, v75
	s_nop 0
	v_add_f32_e32 v74, v74, v75
	v_mov_b32_e32 v75, v74
	s_nop 1
	v_permlane32_swap_b32_e32 v74, v75
	s_nop 0
	v_add_f32_e32 v74, v74, v75
	v_mov_b32_e32 v75, v74
	s_nop 1
	v_permlane16_swap_b32_e32 v74, v75
	s_nop 0
	v_mul_f32_e32 v74, 0x3c000000, v74
	v_mul_f32_e32 v75, 0x3c000000, v75
	v_fma_f32 v75, -v74, v74, v75
	v_add_f32_e32 v75, 0x3727c5ac, v75
	v_rsq_f32_e32 v76, v75
	s_nop 0
	v_mul_f32_e64 v236, -v74, v76
	v_pk_fma_f32 v[62:63], v[62:63], v[76:77], v[236:237] op_sel_hi:[1,0,0]
	v_pk_fma_f32 v[64:65], v[64:65], v[76:77], v[236:237] op_sel_hi:[1,0,0]
	v_pk_fma_f32 v[66:67], v[66:67], v[76:77], v[236:237] op_sel_hi:[1,0,0]
	v_pk_fma_f32 v[68:69], v[68:69], v[76:77], v[236:237] op_sel_hi:[1,0,0]
	ds_write_b128 v123, v[62:65]
	v_pk_fma_f32 v[70:71], v[70:71], v[76:77], v[236:237] op_sel_hi:[1,0,0]
	v_pk_fma_f32 v[72:73], v[72:73], v[76:77], v[236:237] op_sel_hi:[1,0,0]
	ds_write_b128 v123, v[66:69] offset:64
	v_pk_fma_f32 v[78:79], v[78:79], v[76:77], v[236:237] op_sel_hi:[1,0,0]
	v_pk_fma_f32 v[80:81], v[80:81], v[76:77], v[236:237] op_sel_hi:[1,0,0]
	ds_write_b128 v123, v[70:73] offset:128
	v_pk_fma_f32 v[86:87], v[86:87], v[76:77], v[236:237] op_sel_hi:[1,0,0]
	v_pk_fma_f32 v[88:89], v[88:89], v[76:77], v[236:237] op_sel_hi:[1,0,0]
	ds_write_b128 v123, v[78:81] offset:192
	v_pk_fma_f32 v[90:91], v[90:91], v[76:77], v[236:237] op_sel_hi:[1,0,0]
	v_pk_fma_f32 v[92:93], v[92:93], v[76:77], v[236:237] op_sel_hi:[1,0,0]
	ds_write_b128 v123, v[86:89] offset:256
	v_pk_fma_f32 v[148:149], v[148:149], v[76:77], v[236:237] op_sel_hi:[1,0,0]
	v_pk_fma_f32 v[150:151], v[150:151], v[76:77], v[236:237] op_sel_hi:[1,0,0]
	ds_write_b128 v123, v[90:93] offset:320
	v_pk_fma_f32 v[82:83], v[82:83], v[76:77], v[236:237] op_sel_hi:[1,0,0]
	v_pk_fma_f32 v[84:85], v[84:85], v[76:77], v[236:237] op_sel_hi:[1,0,0]
	ds_write_b128 v123, v[148:151] offset:384
	ds_write_b128 v123, v[82:85] offset:448
	ds_read_b128 v[62:65], v121
	ds_read_b128 v[66:69], v121 offset:1088
	ds_read_b128 v[70:73], v121 offset:2176
	ds_read_b128 v[74:77], v121 offset:3264
	ds_read_b128 v[78:81], v121 offset:4352
	ds_read_b128 v[82:85], v121 offset:5440
	ds_read_b128 v[86:89], v121 offset:6528
	ds_read_b128 v[90:93], v121 offset:7616
	v_add_u32_e32 v136, 0xffffe400, v118
	s_waitcnt vmcnt(15) lgkmcnt(7)
	v_pk_fma_f32 v[64:65], v[56:57], v[64:65], v[60:61]
	v_pk_fma_f32 v[62:63], v[54:55], v[62:63], v[58:59]
	buffer_store_dwordx4 v[62:65], v136, s[4:7], 0 offen sc0 nt sc1
	v_cmp_lt_i32_e32 vcc, s8, v0
	s_or_b64 s[0:1], vcc, s[0:1]
	s_waitcnt lgkmcnt(6)
	v_pk_fma_f32 v[64:65], v[56:57], v[68:69], v[60:61]
	v_pk_fma_f32 v[62:63], v[54:55], v[66:67], v[58:59]
	v_add_u32_e32 v66, 0xffffe800, v118
	buffer_store_dwordx4 v[62:65], v66, s[4:7], 0 offen sc0 nt sc1
	v_add_u32_e32 v66, 0xffffec00, v118
	s_waitcnt lgkmcnt(5)
	v_pk_fma_f32 v[64:65], v[56:57], v[72:73], v[60:61]
	v_pk_fma_f32 v[62:63], v[54:55], v[70:71], v[58:59]
	buffer_store_dwordx4 v[62:65], v66, s[4:7], 0 offen sc0 nt sc1
	v_add_u32_e32 v66, 0xfffff000, v118
	s_waitcnt lgkmcnt(4)
	v_pk_fma_f32 v[64:65], v[56:57], v[76:77], v[60:61]
	v_pk_fma_f32 v[62:63], v[54:55], v[74:75], v[58:59]
	buffer_store_dwordx4 v[62:65], v66, s[4:7], 0 offen sc0 nt sc1
	v_add_u32_e32 v66, 0xfffff400, v118
	s_waitcnt lgkmcnt(3)
	v_pk_fma_f32 v[64:65], v[56:57], v[80:81], v[60:61]
	v_pk_fma_f32 v[62:63], v[54:55], v[78:79], v[58:59]
	buffer_store_dwordx4 v[62:65], v66, s[4:7], 0 offen sc0 nt sc1
	v_add_u32_e32 v66, 0xfffff800, v118
	s_waitcnt lgkmcnt(2)
	v_pk_fma_f32 v[64:65], v[56:57], v[84:85], v[60:61]
	v_pk_fma_f32 v[62:63], v[54:55], v[82:83], v[58:59]
	buffer_store_dwordx4 v[62:65], v66, s[4:7], 0 offen sc0 nt sc1
	v_add_u32_e32 v66, 0xfffffc00, v118
	s_waitcnt lgkmcnt(1)
	v_pk_fma_f32 v[64:65], v[56:57], v[88:89], v[60:61]
	v_pk_fma_f32 v[62:63], v[54:55], v[86:87], v[58:59]
	buffer_store_dwordx4 v[62:65], v66, s[4:7], 0 offen sc0 nt sc1
	s_waitcnt lgkmcnt(0)
	s_nop 0
	v_pk_fma_f32 v[64:65], v[56:57], v[92:93], v[60:61]
	v_pk_fma_f32 v[62:63], v[54:55], v[90:91], v[58:59]
	buffer_store_dwordx4 v[62:65], v118, s[4:7], 0 offen sc0 nt sc1
	v_add_u32_e32 v118, 0x1000000, v118
	s_nop 0
	v_mov_b32_e32 v62, v0
	s_waitcnt vmcnt(21)
	v_mov_b32_e32 v64, v135
	s_andn2_b64 exec, exec, s[0:1]
	s_cbranch_execnz .LBB1_6
